# speedup vs baseline: 1.0460x; 1.0021x over previous
_Z6k_histPKfS0_S0_PfPiS1_:
	s_load_dwordx4 s[4:7], s[0:1], 0x0
	s_load_dwordx4 s[8:11], s[0:1], 0x10
	s_load_dwordx4 s[12:15], s[0:1], 0x20
	v_and_b32_e32 v1, 63, v0
	v_readfirstlane_b32 s3, v0
	v_mov_b32_e32 v20, 0
	v_mov_b32_e32 v21, 0
	v_mov_b32_e32 v22, 0
	v_mov_b32_e32 v23, 0
	v_lshlrev_b32_e32 v19, 4, v0
	v_add_u32_e32 v19, 0xc200, v19
	s_lshr_b32 s3, s3, 6
	ds_write_b128 v19, v[20:23]
	ds_write_b128 v19, v[20:23] offset:16384
	ds_write_b128 v19, v[20:23] offset:32768
	ds_write_b128 v19, v[20:23] offset:49152
	s_cmp_gt_u32 s3, 1
	s_cbranch_scc1 .Lh_zero_done
	v_add_u32_e32 v19, 0x10000, v19
	ds_write_b128 v19, v[20:23]

.Lh_no_out:
	s_cmp_eq_u32 s17, 0
	s_cselect_b32 s4, s4, s6
	s_cselect_b32 s5, s5, s7
	s_add_u32 s24, s8, s22
	s_addc_u32 s25, s9, 0
	s_add_u32 s4, s4, s21
	s_addc_u32 s5, s5, 0
	global_load_dwordx4 v[14:17], v18, s[24:25] nt
	global_load_dwordx4 v[2:5], v18, s[4:5] nt
	s_add_u32 s6, s4, 0x40000
	s_addc_u32 s7, s5, 0
	s_add_u32 s8, s4, 0x80000
	s_addc_u32 s9, s5, 0
	s_barrier
	global_load_dwordx4 v[6:9], v18, s[6:7] nt
	s_barrier
	global_load_dwordx4 v[10:13], v18, s[8:9] nt
	s_mul_i32 s46, s3, 0xc00
	s_add_u32 s46, s46, 32
	s_mov_b32 m0, s46
	v_and_b32_e32 v38, 15, v0
	s_mul_i32 s58, s17, 0x8400
	s_add_u32 s58, s58, 0xc580
	v_lshl_add_u32 v38, v38, 3, s58
	v_add_u32_e32 v39, 0x2c00, v38
	v_add_u32_e32 v40, 0x5800, v38
	v_mov_b32_e32 v67, 0
	v_mov_b32_e32 v41, 0x41fc0000
	v_mov_b32_e32 v42, 0xbf38aa3b
	s_mov_b32 s48, 0x3f940000
	s_mov_b32 s51, 0x3fb8aa3b
	s_mov_b32 s42, 0
	s_mov_b32 s43, 0
	s_mov_b32 s44, 0x7fffffff
	s_mov_b32 s45, 0x7fffffff
	s_mov_b32 s47, 0
	s_mul_i32 s58, s3, 0x2c00
	s_add_u32 s58, s58, 0xc500
	v_lshl_add_u32 v44, v1, 7, s58
	v_lshlrev_b32_e32 v49, 2, v1
	s_cmp_lg_u32 s3, 6
	s_cbranch_scc1 .Lh_rows_done
	v_mul_u32_u24_e32 v45, 43, v1
	v_lshrrev_b32_e32 v45, 8, v45
	v_mul_u32_u24_e32 v46, 6, v45
	v_sub_u32_e32 v46, v1, v46
	v_mul_u32_u24_e32 v44, 0x2c00, v45
	v_lshl_add_u32 v44, v46, 7, v44
	v_add_u32_e32 v44, 0xe500, v44
	v_lshlrev_b32_e32 v49, 8, v45
	v_lshl_add_u32 v49, v46, 2, v49
	v_add_u32_e32 v49, 0xe8, v49
.Lh_rows_done:
	v_bfe_u32 v45, v1, 1, 3
	v_lshlrev_b32_e32 v45, 4, v45
	v_xor_b32_e32 v46, 16, v45
	v_xor_b32_e32 v47, 32, v45
	v_xor_b32_e32 v48, 48, v45
	v_xor_b32_e32 v50, 64, v45
	v_xor_b32_e32 v51, 80, v45
	v_xor_b32_e32 v52, 96, v45
	v_xor_b32_e32 v53, 112, v45
	v_add_u32_e32 v45, v44, v45
	v_add_u32_e32 v46, v44, v46
	v_add_u32_e32 v47, v44, v47
	v_add_u32_e32 v48, v44, v48
	v_add_u32_e32 v50, v44, v50
	v_add_u32_e32 v51, v44, v51
	v_add_u32_e32 v52, v44, v52
	v_add_u32_e32 v53, v44, v53
	v_add_u32_e32 v54, 6, v1
	v_and_b32_e32 v54, 63, v54
	v_lshlrev_b32_e32 v54, 2, v54
	s_mul_i32 s58, s2, 0x600
	s_add_u32 s10, s10, s58
	s_addc_u32 s11, s11, 0
	s_lshl_b32 s59, s3, 8
	s_cmp_lt_u32 s3, 6
	s_cselect_b32 s59, s59, 0
	v_add_u32_e32 v49, s59, v49
	s_lshl_b32 s58, s2, 2
	s_add_u32 s12, s12, s58
	s_addc_u32 s13, s13, 0
	s_waitcnt vmcnt(3)
	v_cmp_lt_f32_e64 s[26:27], 0.5, v14
	v_cmp_lt_f32_e64 s[28:29], 0.5, v15
	v_cmp_lt_f32_e64 s[30:31], 0.5, v16
	v_cmp_lt_f32_e64 s[32:33], 0.5, v17
	s_cmp_lg_u32 s17, 0
	s_cbranch_scc1 .Lh_no_cnt
	s_bcnt1_i32_b64 s54, s[26:27]
	s_bcnt1_i32_b64 s55, s[28:29]
	s_bcnt1_i32_b64 s56, s[30:31]
	s_bcnt1_i32_b64 s57, s[32:33]
	s_add_i32 s54, s54, s55
	s_add_i32 s56, s56, s57
	s_add_i32 s54, s54, s56
	s_lshl_b32 s55, s16, 2
	v_mov_b32_e32 v36, s55
	v_mov_b32_e32 v37, s54
	s_mov_b64 exec, 1
	ds_write_b32 v36, v37
	s_mov_b64 exec, -1

.Lh_loop_first:
	ds_read_addtid_b32 v24
	s_waitcnt lgkmcnt(0)
.Lh_loop_body:
	v_fmamk_f32 v27, v24, 0x42000000, v41
	ds_read_addtid_b32 v24 offset:256
	s_sub_i32 s49, s44, s43
	s_sub_i32 s50, s45, s43
	s_add_i32 s43, s43, 64
	v_rndne_f32_e32 v28, v27
	v_cmp_le_i32_e32 vcc, s49, v1
	v_cmp_le_i32_e64 s[52:53], s50, v1
	v_sub_f32_e32 v29, v27, v28
	v_cvt_i32_f32_e32 v30, v28
	v_cndmask_b32_e32 v36, v38, v39, vcc
	v_mul_f32_e32 v37, 0xbf38aa3b, v29
	v_cndmask_b32_e64 v36, v36, v40, s[52:53]
	v_fmamk_f32 v32, v29, 0x3fb8aa3b, v42
	v_fma_f32 v33, -v29, s51, v42
	v_fmaak_f32 v31, v29, v37, 0x41a00000
	v_lshl_add_u32 v30, v30, 7, v36
	v_exp_f32_e32 v31, v31
	v_exp_f32_e32 v32, v32
	v_exp_f32_e32 v33, v33
	v_cvt_rpi_i32_f32_e32 v66, v31
	ds_add_u64 v30, v[66:67] offset:640
	v_mul_f32_e32 v34, v32, v31
	v_mul_f32_e32 v35, v33, v31
	v_cvt_rpi_i32_f32_e32 v57, v34
	v_cvt_rpi_i32_f32_e32 v64, v35
	v_mul_f32_e32 v32, 0x3ebc5ab2, v32
	v_mul_f32_e32 v33, 0x3ebc5ab2, v33
	v_mul_f32_e32 v34, v32, v34
	v_mul_f32_e32 v35, v33, v35
	v_cvt_rpi_i32_f32_e32 v59, v34
	v_cvt_rpi_i32_f32_e32 v62, v35
	v_mul_f32_e32 v32, 0x3ebc5ab2, v32
	v_mul_f32_e32 v33, 0x3ebc5ab2, v33
	v_mul_f32_e32 v34, v32, v34
	v_mul_f32_e32 v35, v33, v35
	v_cvt_rpi_i32_f32_e32 v61, v34
	v_cvt_rpi_i32_f32_e32 v60, v35
	ds_add_u64 v30, v[60:61] offset:256
	v_mul_f32_e32 v32, 0x3ebc5ab2, v32
	v_mul_f32_e32 v33, 0x3ebc5ab2, v33
	v_mul_f32_e32 v34, v32, v34
	v_mul_f32_e32 v35, v33, v35
	v_cvt_rpi_i32_f32_e32 v63, v34
	v_cvt_rpi_i32_f32_e32 v58, v35
	ds_add_u64 v30, v[62:63] offset:384
	ds_add_u64 v30, v[58:59] offset:128
	v_mul_f32_e32 v32, 0x3ebc5ab2, v32
	v_mul_f32_e32 v33, 0x3ebc5ab2, v33
	v_mul_f32_e32 v34, v32, v34
	v_mul_f32_e32 v35, v33, v35
	v_cvt_rpi_i32_f32_e32 v65, v34
	v_cvt_rpi_i32_f32_e32 v56, v35
	ds_add_u64 v30, v[64:65] offset:512
	ds_add_u64 v30, v[56:57]
	s_add_u32 m0, m0, 0x100
	s_sub_i32 s59, s42, s43
	s_cmp_ge_i32 s59, 64
	s_waitcnt lgkmcnt(6)
	s_cbranch_scc1 .Lh_loop_body

.Lh_epilogue:
	s_mov_b64 exec, -1
	s_waitcnt lgkmcnt(0)
	s_barrier
	s_cmp_gt_u32 s3, 7
	s_cbranch_scc1 .Lh_end
	s_cmp_eq_u32 s3, 7
	s_cbranch_scc1 .Lh_pcnt
	ds_read_b128 v[2:5], v45
	ds_read_b128 v[6:9], v46
	ds_read_b128 v[10:13], v47
	ds_read_b128 v[14:17], v48
	ds_read_b128 v[24:27], v50
	ds_read_b128 v[28:31], v51
	ds_read_b128 v[32:35], v52
	ds_read_b128 v[36:39], v53
	s_cmp_eq_u32 s3, 6
	s_cbranch_scc1 .Lh_tailbins
	s_waitcnt lgkmcnt(5)
	v_add3_u32 v2, v2, v4, v6
	v_add3_u32 v3, v3, v5, v7
	v_add3_u32 v8, v8, v10, v12
	v_add3_u32 v9, v9, v11, v13
	s_waitcnt lgkmcnt(2)
	v_add3_u32 v14, v14, v16, v24
	v_add3_u32 v15, v15, v17, v25
	v_add3_u32 v26, v26, v28, v30
	v_add3_u32 v27, v27, v29, v31
	s_waitcnt lgkmcnt(0)
	v_add3_u32 v32, v32, v34, v36
	v_add3_u32 v33, v33, v35, v37
	v_add3_u32 v2, v2, v8, v14
	v_add3_u32 v3, v3, v9, v15
	v_add3_u32 v26, v26, v32, v38
	v_add3_u32 v27, v27, v33, v39
	v_add_u32_e32 v2, v2, v26
	v_add_u32_e32 v3, v3, v27
	ds_bpermute_b32 v4, v54, v2
	s_waitcnt lgkmcnt(0)
	v_add_u32_e32 v3, v3, v4
	v_cvt_f32_u32_e32 v3, v3
	v_mul_f32_e32 v3, 0x35800000, v3
	s_mov_b32 s58, -1
	s_mov_b32 s59, 0x3ffffff
	s_mov_b64 exec, s[58:59]
	global_store_dword v49, v3, s[10:11]
	s_endpgm
.Lh_tailbins:
	v_add_u32_e32 v45, 0xfffffd00, v45
	v_add_u32_e32 v46, 0xfffffd00, v46
	v_add_u32_e32 v47, 0xfffffd00, v47
	v_add_u32_e32 v48, 0xfffffd00, v48
	v_add_u32_e32 v50, 0xfffffd00, v50
	v_add_u32_e32 v51, 0xfffffd00, v51
	v_add_u32_e32 v52, 0xfffffd00, v52
	v_add_u32_e32 v53, 0xfffffd00, v53
	ds_read_b128 v[56:59], v45
	ds_read_b128 v[60:63], v46
	ds_read_b128 v[64:67], v47
	ds_read_b128 v[68:71], v48
	ds_read_b128 v[72:75], v50
	ds_read_b128 v[76:79], v51
	ds_read_b128 v[80:83], v52
	ds_read_b128 v[84:87], v53
	s_waitcnt lgkmcnt(8)
	v_add3_u32 v2, v2, v4, v6
	v_add3_u32 v8, v8, v10, v12
	v_add3_u32 v14, v14, v16, v24
	v_add3_u32 v26, v26, v28, v30
	v_add3_u32 v32, v32, v34, v36
	v_add3_u32 v2, v2, v8, v14
	v_add3_u32 v26, v26, v32, v38
	v_add_u32_e32 v2, v2, v26
	s_waitcnt lgkmcnt(0)
	v_add3_u32 v57, v57, v59, v61
	v_add3_u32 v63, v63, v65, v67
	v_add3_u32 v69, v69, v71, v73
	v_add3_u32 v75, v75, v77, v79
	v_add3_u32 v81, v81, v83, v85
	v_add3_u32 v57, v57, v63, v69
	v_add3_u32 v75, v75, v81, v87
	v_add3_u32 v2, v2, v57, v75
	v_cvt_f32_u32_e32 v2, v2
	v_mul_f32_e32 v2, 0x35800000, v2
	s_mov_b32 s58, -1
	s_mov_b32 s59, 15
	s_mov_b64 exec, s[58:59]
	global_store_dword v49, v2, s[10:11]
	s_endpgm

	.amdhsa_kernel _Z6k_histPKfS0_S0_PfPiS1_
		.amdhsa_group_segment_fixed_size 34048
		.amdhsa_private_segment_fixed_size 0
		.amdhsa_kernarg_size 48
		.amdhsa_user_sgpr_count 2
		.amdhsa_user_sgpr_dispatch_ptr 0
		.amdhsa_user_sgpr_queue_ptr 0
		.amdhsa_user_sgpr_kernarg_segment_ptr 1
		.amdhsa_user_sgpr_dispatch_id 0
		.amdhsa_user_sgpr_kernarg_preload_length 0
		.amdhsa_user_sgpr_kernarg_preload_offset 0
		.amdhsa_user_sgpr_private_segment_size 0
		.amdhsa_uses_dynamic_stack 0
		.amdhsa_enable_private_segment 0
		.amdhsa_system_sgpr_workgroup_id_x 1
		.amdhsa_system_sgpr_workgroup_id_y 0
		.amdhsa_system_sgpr_workgroup_id_z 0
		.amdhsa_system_sgpr_workgroup_info 0
		.amdhsa_system_vgpr_workitem_id 0
		.amdhsa_next_free_vgpr 88
		.amdhsa_next_free_sgpr 60
		.amdhsa_accum_offset 88
		.amdhsa_reserve_vcc 1
		.amdhsa_float_round_mode_32 0
		.amdhsa_float_round_mode_16_64 0
		.amdhsa_float_denorm_mode_32 3
		.amdhsa_float_denorm_mode_16_64 3
		.amdhsa_dx10_clamp 1
		.amdhsa_ieee_mode 1
		.amdhsa_fp16_overflow 0
		.amdhsa_tg_split 0
		.amdhsa_exception_fp_ieee_invalid_op 0
		.amdhsa_exception_fp_denorm_src 0
		.amdhsa_exception_fp_ieee_div_zero 0
		.amdhsa_exception_fp_ieee_overflow 0
		.amdhsa_exception_fp_ieee_underflow 0
		.amdhsa_exception_fp_ieee_inexact 0
		.amdhsa_exception_int_div_zero 0
	.end_amdhsa_kernel

.Lfunc_end0:
	.size	_Z6k_histPKfS0_S0_PfPiS1_, .Lfunc_end0-_Z6k_histPKfS0_S0_PfPiS1_
	.set _Z6k_histPKfS0_S0_PfPiS1_.num_vgpr, 88
	.set _Z6k_histPKfS0_S0_PfPiS1_.num_agpr, 0
	.set _Z6k_histPKfS0_S0_PfPiS1_.numbered_sgpr, 60
	.set _Z6k_histPKfS0_S0_PfPiS1_.num_named_barrier, 0
	.set _Z6k_histPKfS0_S0_PfPiS1_.private_seg_size, 0
	.set _Z6k_histPKfS0_S0_PfPiS1_.uses_vcc, 1
	.set _Z6k_histPKfS0_S0_PfPiS1_.uses_flat_scratch, 0
	.set _Z6k_histPKfS0_S0_PfPiS1_.has_dyn_sized_stack, 0
	.set _Z6k_histPKfS0_S0_PfPiS1_.has_recursion, 0
	.set _Z6k_histPKfS0_S0_PfPiS1_.has_indirect_call, 0

amdhsa.kernels:
  - .agpr_count:     0
    .args:
      - .actual_access:  read_only
        .address_space:  global
        .offset:         0
        .size:           8
        .value_kind:     global_buffer
      - .actual_access:  read_only
        .address_space:  global
        .offset:         8
        .size:           8
        .value_kind:     global_buffer
      - .actual_access:  read_only
        .address_space:  global
        .offset:         16
        .size:           8
        .value_kind:     global_buffer
      - .actual_access:  write_only
        .address_space:  global
        .offset:         24
        .size:           8
        .value_kind:     global_buffer
      - .actual_access:  write_only
        .address_space:  global
        .offset:         32
        .size:           8
        .value_kind:     global_buffer
      - .actual_access:  write_only
        .address_space:  global
        .offset:         40
        .size:           8
        .value_kind:     global_buffer
    .group_segment_fixed_size: 34048
    .kernarg_segment_align: 8
    .kernarg_segment_size: 48
    .language:       OpenCL C
    .language_version:
      - 2
      - 0
    .max_flat_workgroup_size: 1024
    .name:           _Z6k_histPKfS0_S0_PfPiS1_
    .private_segment_fixed_size: 0
    .sgpr_count:     66
    .sgpr_spill_count: 0
    .symbol:         _Z6k_histPKfS0_S0_PfPiS1_.kd
    .uniform_work_group_size: 1
    .uses_dynamic_stack: false
    .vgpr_count:     88
    .vgpr_spill_count: 0
    .wavefront_size: 64
  - .agpr_count:     0
    .args:
      - .actual_access:  read_only
        .address_space:  global
        .offset:         0
        .size:           8
        .value_kind:     global_buffer
      - .actual_access:  read_only
        .address_space:  global
        .offset:         8
        .size:           8
        .value_kind:     global_buffer
      - .address_space:  global
        .offset:         16
        .size:           8
        .value_kind:     global_buffer
    .group_segment_fixed_size: 2080
    .kernarg_segment_align: 8
    .kernarg_segment_size: 24
    .language:       OpenCL C
    .language_version:
      - 2
      - 0
    .max_flat_workgroup_size: 256
    .name:           _Z7k_finalPKfPKiPf
    .private_segment_fixed_size: 0
    .sgpr_count:     18
    .sgpr_spill_count: 0
    .symbol:         _Z7k_finalPKfPKiPf.kd
    .uniform_work_group_size: 1
    .uses_dynamic_stack: false
    .vgpr_count:     40
    .vgpr_spill_count: 0
    .wavefront_size: 64
